# mfix+route prefix+acc zeroing removal+cv split retune, plus window-attention sink logit load no longer stalls unit set-up
# speedup vs baseline: 1.0058x; 1.0058x over previous
.LBB0_1061:
	s_cmp_eq_u32 s12, 0
	s_mov_b32 s8, 35
	s_cselect_b64 s[24:25], -1, 0
	s_ashr_i32 s9, s8, 31
	s_lshl_b64 s[8:9], s[8:9], 3
	s_add_u32 s8, s0, s8
	s_addc_u32 s9, s1, s9
	s_mov_b32 s10, 35
	s_load_dwordx2 s[8:9], s[8:9], 0x0
	s_ashr_i32 s11, s10, 31
	s_lshl_b64 s[10:11], s[10:11], 3
	s_add_u32 s10, s0, s10
	s_addc_u32 s11, s1, s11
	s_load_dwordx2 s[10:11], s[10:11], 0x0
	s_and_b64 vcc, exec, s[24:25]
	v_mov_b32_e32 v233, 0xff800000
	s_cbranch_vccnz .LBB0_1063
	s_mov_b32 s26, 23
	s_ashr_i32 s27, s26, 31
	s_lshl_b64 s[26:27], s[26:27], 3
	s_add_u32 s26, s0, s26
	s_addc_u32 s27, s1, s27
	s_load_dwordx2 s[26:27], s[26:27], 0x0
	s_mul_i32 s28, s73, 6
	s_add_i32 s28, s13, s28
	s_ashr_i32 s29, s28, 31
	s_lshl_b64 s[28:29], s[28:29], 2
	s_waitcnt lgkmcnt(0)
	s_add_u32 s26, s26, s28
	s_addc_u32 s27, s27, s29
	global_load_dword v233, v1, s[26:27]

.LBB0_1149:
	v_add_f32_e32 v2, v96, v97
	v_add_f32_e32 v2, v98, v2
	v_add_f32_e32 v2, v99, v2
	v_add_f32_e32 v2, v100, v2
	v_add_f32_e32 v2, v101, v2
	v_add_f32_e32 v2, v102, v2
	v_add_f32_e32 v2, v103, v2
	v_add_f32_e32 v2, v104, v2
	v_add_f32_e32 v2, v105, v2
	v_add_f32_e32 v2, v106, v2
	v_add_f32_e32 v2, v107, v2
	v_add_f32_e32 v2, v108, v2
	v_add_f32_e32 v2, v109, v2
	v_add_f32_e32 v2, v110, v2
	v_add_f32_e32 v2, v111, v2
	v_add_f32_e32 v2, v48, v2
	v_add_f32_e32 v2, v49, v2
	v_add_f32_e32 v2, v50, v2
	v_add_f32_e32 v2, v51, v2
	v_add_f32_e32 v2, v52, v2
	v_add_f32_e32 v2, v53, v2
	v_add_f32_e32 v2, v54, v2
	v_add_f32_e32 v2, v55, v2
	v_add_f32_e32 v2, v56, v2
	v_add_f32_e32 v2, v57, v2
	v_add_f32_e32 v2, v58, v2
	v_add_f32_e32 v2, v59, v2
	v_add_f32_e32 v2, v60, v2
	v_add_f32_e32 v2, v61, v2
	s_cmp_lg_u32 0, -1
	v_add_f32_e32 v2, v62, v2
	s_cselect_b32 s8, 0, 0
	v_add_f32_e32 v2, v63, v2
	s_addk_i32 s8, 0x6000
	v_add_f32_e32 v0, v0, v2
	v_cvt_pk_bf16_f32 v2, v96, v97
	v_cvt_pk_bf16_f32 v3, v98, v99
	v_cvt_pk_bf16_f32 v4, v100, v101
	v_cvt_pk_bf16_f32 v5, v102, v103
	v_cvt_pk_bf16_f32 v6, v104, v105
	v_cvt_pk_bf16_f32 v7, v106, v107
	v_cvt_pk_bf16_f32 v8, v108, v109
	v_cvt_pk_bf16_f32 v9, v110, v111
	v_cvt_pk_bf16_f32 v10, v48, v49
	v_cvt_pk_bf16_f32 v11, v50, v51
	v_cvt_pk_bf16_f32 v12, v52, v53
	v_cvt_pk_bf16_f32 v13, v54, v55
	v_cvt_pk_bf16_f32 v48, v56, v57
	v_cvt_pk_bf16_f32 v49, v58, v59
	v_cvt_pk_bf16_f32 v50, v60, v61
	v_cvt_pk_bf16_f32 v51, v62, v63
	v_add3_u32 v14, v236, s8, v237
	v_add3_u32 v14, v14, v234, s70
	ds_read_b64_tr_b16 v[52:53],v14 offset:0
	ds_read_b64_tr_b16 v[54:55],v14 offset:512
	ds_read_b64_tr_b16 v[56:57],v14 offset:1024
	ds_read_b64_tr_b16 v[58:59],v14 offset:1536
	ds_read_b64_tr_b16 v[60:61],v14 offset:2048
	ds_read_b64_tr_b16 v[62:63],v14 offset:2560
	ds_read_b64_tr_b16 v[64:65],v14 offset:3072
	ds_read_b64_tr_b16 v[66:67],v14 offset:3584
	s_waitcnt lgkmcnt(0)
	s_nop 0
	v_mfma_f32_32x32x16_bf16 v[32:47], v[2:5], v[52:55], v[32:47]
	ds_read_b64_tr_b16 v[52:53],v14 offset:4096
	ds_read_b64_tr_b16 v[54:55],v14 offset:4608
	v_mfma_f32_32x32x16_bf16 v[32:47], v[6:9], v[56:59], v[32:47]
	ds_read_b64_tr_b16 v[56:57],v14 offset:5120
	ds_read_b64_tr_b16 v[58:59],v14 offset:5632
	v_mfma_f32_32x32x16_bf16 v[32:47], v[10:13], v[60:63], v[32:47]
	ds_read_b64_tr_b16 v[60:61],v14 offset:6144
	ds_read_b64_tr_b16 v[62:63],v14 offset:6656
	v_mfma_f32_32x32x16_bf16 v[32:47], v[48:51], v[64:67], v[32:47]
	ds_read_b64_tr_b16 v[64:65],v14 offset:7168
	ds_read_b64_tr_b16 v[66:67],v14 offset:7680
	s_waitcnt lgkmcnt(0)
	v_mfma_f32_32x32x16_bf16 v[16:31], v[2:5], v[52:55], v[16:31]
	v_mul_f32_e32 v2, 0x3fb8aa3b, v233
	v_sub_f32_e32 v2, v2, v235
	v_exp_f32_e32 v2, v2
	v_cmp_gt_u32_e32 vcc, 32, v211
	v_add_f32_e32 v2, v2, v0
	s_nop 0
	v_cndmask_b32_e32 v0, v0, v2, vcc
	v_mfma_f32_32x32x16_bf16 v[16:31], v[6:9], v[56:59], v[16:31]
	v_mov_b32_e32 v2, v0
	s_nop 1
	v_permlane32_swap_b32_e32 v0, v2
	v_mfma_f32_32x32x16_bf16 v[16:31], v[10:13], v[60:63], v[16:31]
	v_mfma_f32_32x32x16_bf16 v[16:31], v[48:51], v[64:67], v[16:31]
	s_and_saveexec_b64 s[8:9], vcc
	s_cbranch_execz .LBB0_979
	v_add_f32_e32 v0, v0, v2
	ds_write_b32 v239, v0 offset:49280
	s_branch .LBB0_979
